# stack: v23 plus P6 H warm-up, P2 cross-unit prefetch, pipelined P3 scan, P4 D-skip pointer hoist
# baseline (speedup 1.0000x reference)
; #define LAS __attribute__((address_space(3)))
; __device__ __forceinline__ float bf2f(bf16 b) { return __uint_as_float(((unsigned)b) << 16); }
; __device__ __forceinline__ float softplus_f(float x) { return x > 20.f ? x : log1pf(__expf(x)); }
; __device__ __forceinline__ void p4_ssd(Ctx& X, int unit) {
;     const int c = unit >> 1, g = unit & 1, t0 = c * CH, tid = X.tid, lane = X.lane, w = X.wave;
;     LAS uchar* Cc = X.lds; LAS uchar* Bc = X.lds + 34816;
;     LAS uchar* HP = X.lds + 34816;
;     LAS float* dtS = (LAS float*)(X.lds + 110592); LAS float* acS = (LAS float*)(X.lds + 114688);
;     const int fr = lane & 15, fq = lane >> 4, q4 = (lane & 15) >> 2, p4 = lane & 3, l = 16 * w + fr;
;     const bf16* zp = PROJ_AT(X, t0 + l, C_Z + 512 * g) + 4 * fq;
;     const int hd = 8 * g + w, l0 = 2 * lane;
;     const bf16 dr0 = *PROJ_AT(X, t0 + l0, C_DT + hd), dr1 = *PROJ_AT(X, t0 + l0 + 1, C_DT + hd);
;     u32x4 bcv[8];
; #pragma unroll
;     for (int i = 0; i < 4; ++i) { const int q = tid + 512 * i, l_ = q >> 4, nc = q & 15;
;         bcv[2 * i] = __builtin_nontemporal_load((const u32x4*)(XP_XBC(X) + (size_t)(t0 + l_) * XBCW + 1024 + 128 * g + nc * 8));
;         bcv[2 * i + 1] = __builtin_nontemporal_load((const u32x4*)(XP_XBC(X) + (size_t)(t0 + l_) * XBCW + 1280 + 128 * g + nc * 8)); }
;     u32x4 px[4], ps[4];
; #pragma unroll
;     for (int i = 0; i < 4; ++i) { const int q = tid + 512 * i; { const int e2 = q >> 10, s_ = (q >> 3) & 127, pc = q & 7; px[i] = __builtin_nontemporal_load((const u32x4*)(XP_XBC(X) + (size_t)(t0 + s_) * XBCW + 512 * g + 64 * e2 + pc * 8)); }
;         { const int e2 = q >> 10, p = (q >> 4) & 63, nc = q & 15; ps[i] = __builtin_nontemporal_load((const u32x4*)(XP_SST(X) + ((size_t)(c * 16 + 8 * g + e2) * 64 + p) * 128 + nc * 8)); } }
;     u32x2 zq[2][4];
; #pragma unroll
;     for (int e2 = 0; e2 < 2; ++e2)
; #pragma unroll
;         for (int n = 0; n < 4; ++n) zq[e2][n] = __builtin_nontemporal_load((const u32x2*)(zp + 64 * e2 + 16 * n));
;     { const float dtb = XP_dt_bias(X)[hd], A = -expf(XP_a_log(X)[hd]);
;       const float d0 = softplus_f(bf2f(dr0) + dtb), d1 = softplus_f(bf2f(dr1) + dtb);
;       const float a0 = d0 * A, a1 = d1 * A, incl = wave_incl_scan(a0 + a1, lane);
;       dtS[w * 128 + l0] = d0; dtS[w * 128 + l0 + 1] = d1; acS[w * 128 + l0] = incl - a1; acS[w * 128 + l0 + 1] = incl; }
.LBB0_574:
	s_load_dwordx4 s[88:91], s[0:1], 0x98
	s_load_dwordx2 s[98:99], s[0:1], 0x40
	s_load_dword s92, s[0:1], 0xb0
	v_readlane_b32 s2, v248, 9
	s_cmpk_gt_i32 s2, 0x7f
	v_readlane_b32 s93, v248, 4
	s_cbranch_scc1 .LBB0_661
	s_waitcnt lgkmcnt(0)
	s_add_u32 s2, s90, 0x14000000
	v_writelane_b32 v248, s2, 12
	s_addc_u32 s2, s91, 0
	v_writelane_b32 v248, s2, 13
	s_add_u32 s2, s90, 0xa000000
	v_writelane_b32 v248, s2, 14
	s_addc_u32 s2, s91, 0
	v_writelane_b32 v248, s2, 16
	s_add_u32 s2, s90, 0xe000000
	v_lshlrev_b32_e32 v9, 4, v0
	v_mov_b32_e32 v101, 0
	v_and_b32_e32 v2, 0x78, v158
	v_or_b32_e32 v5, 0x200, v0
	s_addc_u32 s3, s91, 0
	v_and_b32_e32 v100, 0x1f00, v9
	v_lshrrev_b32_e32 v166, 4, v5
	v_lshl_add_u64 v[6:7], s[2:3], 0, v[100:101]
	v_lshlrev_b32_e32 v100, 1, v2
	v_lshrrev_b32_e32 v170, 3, v5
	v_lshlrev_b32_e32 v5, 4, v5
	v_or_b32_e32 v8, 0x600, v0
	v_lshl_add_u64 v[102:103], v[6:7], 0, v[100:101]
	v_and_b32_e32 v6, 0x3f00, v5
	v_mov_b32_e32 v7, v101
	v_lshl_add_u64 v[6:7], s[2:3], 0, v[6:7]
	v_lshlrev_b32_e32 v5, 4, v8
	v_lshl_add_u64 v[104:105], v[6:7], 0, v[100:101]
	v_and_b32_e32 v6, 0x3f00, v5
	v_mov_b32_e32 v7, v101
	v_lshl_add_u64 v[6:7], s[2:3], 0, v[6:7]
	v_cmp_eq_u32_e64 s[2:3], 0, v194
	v_lshl_add_u64 v[106:107], v[6:7], 0, v[100:101]
	v_mbcnt_lo_u32_b32 v6, -1, 0
	v_writelane_b32 v248, s2, 18
	v_mbcnt_hi_u32_b32 v6, -1, v6
	v_and_b32_e32 v7, 64, v6
	v_writelane_b32 v248, s3, 19
	v_cmp_gt_u32_e64 s[2:3], 2, v194
	s_waitcnt vmcnt(5)
	v_add_u32_e32 v10, -1, v6
	v_cmp_lt_i32_e32 vcc, v10, v7
	v_writelane_b32 v248, s2, 20
	v_and_b32_e32 v3, 15, v0
	v_cndmask_b32_e32 v10, v10, v6, vcc
	v_writelane_b32 v248, s3, 21
	v_cmp_gt_u32_e64 s[2:3], 4, v194
	v_lshlrev_b32_e32 v172, 2, v10
	v_add_u32_e32 v10, -2, v6
	v_writelane_b32 v248, s2, 22
	v_cmp_lt_i32_e32 vcc, v10, v7
	v_and_b32_e32 v98, 12, v123
	v_writelane_b32 v248, s3, 23
	v_cmp_gt_u32_e64 s[2:3], 8, v194
	v_cndmask_b32_e32 v10, v10, v6, vcc
	v_lshlrev_b32_e32 v173, 2, v10
	v_writelane_b32 v248, s2, 24
	v_add_u32_e32 v10, -4, v6
	v_cmp_lt_i32_e32 vcc, v10, v7
	v_writelane_b32 v248, s3, 25
	v_cmp_gt_u32_e64 s[2:3], 16, v194
	v_cndmask_b32_e32 v10, v10, v6, vcc
	v_lshl_or_b32 v99, s93, 4, v3
	v_writelane_b32 v248, s2, 26
	v_lshlrev_b32_e32 v174, 2, v10
	v_add_u32_e32 v10, -8, v6
	v_writelane_b32 v248, s3, 27
	v_cmp_gt_u32_e64 s[2:3], 32, v194
	v_or_b32_e32 v29, 50, v98
	v_cmp_lt_i32_e32 vcc, v10, v7
	v_writelane_b32 v248, s2, 28
	v_cmp_gt_u32_e64 s[46:47], v29, v99
	v_or_b32_e32 v29, 51, v123
	v_writelane_b32 v248, s3, 29
	s_add_i32 s2, 0, 0x1b000
	s_add_i32 s3, 0, 0x1c000
	s_cmp_gt_u32 s13, 63
	s_cselect_b64 s[6:7], -1, 0
	v_writelane_b32 v248, s6, 30
	s_cmpk_gt_u32 s13, 0x7f
	v_cndmask_b32_e32 v10, v10, v6, vcc
	v_writelane_b32 v248, s7, 31
	s_cselect_b64 s[6:7], -1, 0
	v_writelane_b32 v248, s6, 32
	s_cmpk_gt_u32 s13, 0xbf
	v_cmp_gt_u32_e64 s[48:49], v29, v99
	v_writelane_b32 v248, s7, 33
	s_cselect_b64 s[6:7], -1, 0
	v_writelane_b32 v248, s6, 34
	s_cmpk_gt_u32 s13, 0xff
	v_or_b32_e32 v29, 64, v98
	v_writelane_b32 v248, s7, 35
	s_cselect_b64 s[6:7], -1, 0
	v_writelane_b32 v248, s6, 36
	s_cmpk_gt_u32 s13, 0x13f
	v_lshlrev_b32_e32 v175, 2, v10
	v_add_u32_e32 v10, -16, v6
	v_writelane_b32 v248, s7, 37
	s_cselect_b64 s[6:7], -1, 0
	v_cmp_gt_u32_e64 s[50:51], v29, v99
	v_cmp_lt_u32_e64 s[52:53], v29, v99
	v_or_b32_e32 v29, 0x42, v98
	v_cmp_lt_i32_e32 vcc, v10, v7
	v_writelane_b32 v248, s6, 38
	s_cmpk_gt_u32 s13, 0x17f
	v_cmp_gt_u32_e64 s[54:55], v29, v99
	v_or_b32_e32 v29, 0x43, v123
	v_cndmask_b32_e32 v10, v10, v6, vcc
	v_writelane_b32 v248, s7, 39
	s_cselect_b64 s[6:7], -1, 0
	v_cmp_gt_u32_e64 s[56:57], v29, v99
	v_or_b32_e32 v29, 0x50, v98
	v_lshlrev_b32_e32 v176, 2, v10
	v_subrev_u32_e32 v10, 32, v6
	v_writelane_b32 v248, s6, 40
	s_cmpk_gt_u32 s13, 0x1bf
	v_cmp_gt_u32_e64 s[58:59], v29, v99
	v_cmp_lt_u32_e64 s[60:61], v29, v99
	v_or_b32_e32 v29, 0x52, v98
	v_cmp_lt_i32_e32 vcc, v10, v7
	v_and_b32_e32 v16, 48, v0
	v_writelane_b32 v248, s7, 41
	s_cselect_b64 s[96:97], -1, 0
	s_add_i32 s6, 0, 0x11800
	v_cmp_gt_u32_e64 s[62:63], v29, v99
	v_or_b32_e32 v29, 0x53, v123
	v_cndmask_b32_e32 v10, v10, v6, vcc
	s_waitcnt vmcnt(4)
; __device__ __forceinline__ void p4_ssd(Ctx& X, int unit) {
;     const int c = unit >> 1, g = unit & 1, t0 = c * CH, tid = X.tid, lane = X.lane, w = X.wave;
;     LAS uchar* Cc = X.lds; LAS uchar* Bc = X.lds + 34816;
;     LAS uchar* HP = X.lds + 34816;
;     LAS float* dtS = (LAS float*)(X.lds + 110592); LAS float* acS = (LAS float*)(X.lds + 114688);
;     const int fr = lane & 15, fq = lane >> 4, q4 = (lane & 15) >> 2, p4 = lane & 3, l = 16 * w + fr;
;     const bf16* zp = PROJ_AT(X, t0 + l, C_Z + 512 * g) + 4 * fq;
;     const int hd = 8 * g + w, l0 = 2 * lane;
;     const bf16 dr0 = *PROJ_AT(X, t0 + l0, C_DT + hd), dr1 = *PROJ_AT(X, t0 + l0 + 1, C_DT + hd);
;     u32x4 bcv[8];
; #pragma unroll
;     for (int i = 0; i < 4; ++i) { const int q = tid + 512 * i, l_ = q >> 4, nc = q & 15;
;         bcv[2 * i] = __builtin_nontemporal_load((const u32x4*)(XP_XBC(X) + (size_t)(t0 + l_) * XBCW + 1024 + 128 * g + nc * 8));
;         bcv[2 * i + 1] = __builtin_nontemporal_load((const u32x4*)(XP_XBC(X) + (size_t)(t0 + l_) * XBCW + 1280 + 128 * g + nc * 8)); }
;     u32x4 px[4], ps[4];
; #pragma unroll
;     for (int i = 0; i < 4; ++i) { const int q = tid + 512 * i; { const int e2 = q >> 10, s_ = (q >> 3) & 127, pc = q & 7; px[i] = __builtin_nontemporal_load((const u32x4*)(XP_XBC(X) + (size_t)(t0 + s_) * XBCW + 512 * g + 64 * e2 + pc * 8)); }
;         { const int e2 = q >> 10, p = (q >> 4) & 63, nc = q & 15; ps[i] = __builtin_nontemporal_load((const u32x4*)(XP_SST(X) + ((size_t)(c * 16 + 8 * g + e2) * 64 + p) * 128 + nc * 8)); } }
;     u32x2 zq[2][4];
; #pragma unroll
;     for (int e2 = 0; e2 < 2; ++e2)
; #pragma unroll
;         for (int n = 0; n < 4; ++n) zq[e2][n] = __builtin_nontemporal_load((const u32x2*)(zp + 64 * e2 + 16 * n));
;     { const float dtb = XP_dt_bias(X)[hd], A = -expf(XP_a_log(X)[hd]);
;       const float d0 = softplus_f(bf2f(dr0) + dtb), d1 = softplus_f(bf2f(dr1) + dtb);
;       const float a0 = d0 * A, a1 = d1 * A, incl = wave_incl_scan(a0 + a1, lane);
;       dtS[w * 128 + l0] = d0; dtS[w * 128 + l0 + 1] = d1; acS[w * 128 + l0] = incl - a1; acS[w * 128 + l0 + 1] = incl; }
; #pragma unroll
;     for (int i = 0; i < 4; ++i) { const int q = tid + 512 * i, l_ = q >> 4, nc = q & 15;
;         *(LAS u32x4*)(Bc + l_ * 272 + nc * 16) = bcv[2 * i];
;         *(LAS u32x4*)(Cc + l_ * 272 + nc * 16) = bcv[2 * i + 1]; }
;     __syncthreads();
	v_add_u32_e32 v19, s6, v16
	v_mov_b32_e32 v22, s6
	s_add_i32 s6, 0, 0x15c00
	v_cmp_gt_u32_e64 s[64:65], v29, v99
	v_or_b32_e32 v29, 0x60, v98
	v_lshlrev_b32_e32 v177, 2, v10
	v_lshlrev_b32_e32 v10, 3, v194
	v_mov_b32_e32 v26, s6
	s_movk_i32 s6, 0x4800
	v_cmp_gt_u32_e64 s[66:67], v29, v99
	v_cmp_lt_u32_e64 s[68:69], v29, v99
	v_or_b32_e32 v29, 0x62, v98
	v_lshrrev_b32_e32 v169, 3, v0
	v_bfe_u32 v171, v8, 3, 7
	v_lshl_or_b32 v10, s93, 9, v10
	s_movk_i32 s4, 0x90
	v_mad_u32_u24 v27, 1, s6, 0
	v_cmp_gt_u32_e64 s[70:71], v29, v99
	v_or_b32_e32 v29, 0x63, v123
	v_lshrrev_b32_e32 v165, 4, v0
	v_add_u32_e32 v179, s3, v10
	s_movk_i32 s3, 0x110
	v_mul_lo_u32 v20, v99, s4
	v_mad_u32_u24 v21, v169, s4, 0
	v_mad_u32_u24 v24, v170, s4, 0
	v_mad_u32_u24 v27, v171, s4, v27
	s_movk_i32 s4, 0x4400
	v_cmp_gt_u32_e64 s[72:73], v29, v99
	v_or_b32_e32 v29, 0x70, v98
	v_readlane_b32 s11, v248, 9
	v_lshrrev_b32_e32 v168, 4, v8
	v_mad_u32_u24 v23, v165, s3, v22
	v_mad_u32_u24 v25, v166, s3, v22
	v_bfe_u32 v8, v8, 4, 6
	v_mad_u32_u24 v22, 1, s4, v22
	v_cmp_gt_u32_e64 s[74:75], v29, v99
	v_cmp_lt_u32_e64 s[76:77], v29, v99
	v_or_b32_e32 v29, 0x72, v98
	s_bitcmp1_b32 s11, 0
	v_add_u32_e32 v178, s2, v10
	v_mul_lo_u32 v15, v99, s3
	v_mad_u32_u24 v26, v165, s3, v26
	v_mad_u32_u24 v8, v8, s3, v22
	v_cmp_gt_u32_e64 s[78:79], v29, v99
	v_or_b32_e32 v29, 0x73, v123
	v_lshl_add_u32 v184, v98, 2, s2
	s_cselect_b64 s[2:3], -1, 0
	s_bitcmp1_b32 s92, 0
	v_bfe_u32 v5, v0, 2, 2
	v_cmp_gt_u32_e64 s[80:81], v29, v99
	v_xor_b32_e32 v29, 16, v6
	v_add_u32_e32 v7, 64, v7
	s_cselect_b64 s[6:7], -1, 0
	v_or_b32_e32 v5, v98, v5
	v_cmp_lt_i32_e32 vcc, v29, v7
	v_writelane_b32 v248, s6, 42
	v_mul_u32_u24_e32 v5, 0x90, v5
	v_and_b32_e32 v18, 24, v158
	v_cndmask_b32_e32 v29, v6, v29, vcc
	v_writelane_b32 v248, s7, 43
	s_add_u32 s6, s90, 0xa000100
	v_add3_u32 v180, 0, v5, v18
	v_or_b32_e32 v5, 2, v98
	v_or_b32_e32 v18, 18, v98
	v_or_b32_e32 v28, 34, v98
	v_lshlrev_b32_e32 v182, 2, v29
	v_xor_b32_e32 v29, 32, v6
	s_addc_u32 s7, s91, 0
	v_cmp_gt_u32_e64 s[20:21], v5, v99
	v_or_b32_e32 v5, 3, v123
	v_cmp_gt_u32_e64 s[28:29], v18, v99
	v_or_b32_e32 v18, 19, v123
	v_cmp_gt_u32_e64 s[38:39], v28, v99
	v_or_b32_e32 v28, 35, v123
	v_cmp_lt_i32_e32 vcc, v29, v7
	v_writelane_b32 v248, s6, 44
	v_and_b32_e32 v10, 0xf0, v9
	v_cmp_gt_u32_e64 s[22:23], v5, v99
	v_or_b32_e32 v5, 16, v98
	v_cmp_gt_u32_e64 s[30:31], v18, v99
	v_or_b32_e32 v18, 32, v98
	v_cmp_gt_u32_e64 s[40:41], v28, v99
	v_or_b32_e32 v28, 48, v98
	v_cndmask_b32_e32 v6, v6, v29, vcc
	v_writelane_b32 v248, s7, 45
	s_add_u32 s6, s90, 0xa000180
	v_and_b32_e32 v4, 56, v158
	v_add_u32_e32 v11, 0, v10
	v_mul_u32_u24_e32 v12, 0x110, v165
	v_mul_u32_u24_e32 v13, 0x110, v166
	v_mul_u32_u24_e32 v14, 0x110, v168
	v_add_u32_e32 v15, 0, v15
	v_add_u32_e32 v17, 0, v16
	v_mul_u32_u24_e32 v3, 0x110, v3
	v_and_b32_e32 v9, 0x70, v9
	v_lshlrev_b32_e32 v22, 1, v98
	v_cmp_gt_u32_e64 s[24:25], v5, v99
	v_cmp_lt_u32_e64 s[26:27], v5, v99
	v_cmp_gt_u32_e64 s[34:35], v18, v99
	v_cmp_lt_u32_e64 s[36:37], v18, v99
	v_cmp_gt_u32_e64 s[42:43], v28, v99
	v_cmp_lt_u32_e64 s[44:45], v28, v99
	v_add_u32_e32 v20, 0, v20
	v_lshlrev_b32_e32 v5, 1, v5
	v_lshlrev_b32_e32 v18, 1, v18
	v_lshlrev_b32_e32 v28, 1, v28
	v_lshlrev_b32_e32 v183, 2, v6
	v_and_b32_e32 v6, 7, v0
	s_addc_u32 s7, s91, 0
	v_lshlrev_b32_e32 v164, 1, v194
	v_or_b32_e32 v167, 64, v165
	s_mov_b32 s5, 0
	v_cmp_gt_u32_e64 s[16:17], v98, v99
	v_cmp_lt_u32_e64 s[18:19], v98, v99
	v_add_u32_e32 v181, 0xd000, v180
	v_lshlrev_b32_e32 v108, 4, v6
	v_mov_b32_e32 v109, v101
	v_writelane_b32 v248, s6, 46
	s_movk_i32 s33, 0xc00
	v_lshlrev_b32_e32 v100, 1, v2
	s_mov_b32 s10, 0xa000000
	v_lshlrev_b32_e32 v110, 1, v4
	v_mov_b32_e32 v112, 0x80
	v_lshlrev_b32_e32 v114, 1, v98
	s_mov_b32 s94, 0x41a00000
	v_mov_b32_e32 v185, 0x3ecc95a3
	v_add_u32_e32 v186, v11, v12
	v_add_u32_e32 v187, v11, v13
	v_add_u32_e32 v188, v11, v14
	v_add_u32_e32 v189, v21, v9
	v_add_u32_e32 v190, v23, v10
	v_add_u32_e32 v191, v24, v9
	v_add_u32_e32 v192, v25, v10
	v_add_u32_e32 v193, v26, v10
	v_add_u32_e32 v195, v27, v9
	v_add_u32_e32 v196, v8, v10
	s_mov_b64 s[8:9], 0x100
	v_mov_b32_e32 v197, 0x358637bd
	v_mov_b32_e32 v116, 0x3f317218
	v_mov_b32_e32 v198, 0x7f800000
	v_mov_b32_e32 v199, 0x7fc00000
	v_mov_b32_e32 v200, 0xff800000
	v_add_u32_e32 v201, v15, v16
	v_add_u32_e32 v202, v17, v3
	v_add_u32_e32 v203, v19, v3
	v_add_u32_e32 v204, v20, v22
	v_add_u32_e32 v205, v20, v5
	v_add_u32_e32 v206, v20, v18
	v_add_u32_e32 v207, v20, v28
	v_writelane_b32 v248, s7, 47
	s_branch .LBB0_577

; #define LAS __attribute__((address_space(3)))
; __device__ __forceinline__ unsigned pk_bf16(float lo, float hi) { unsigned r; asm("v_cvt_pk_bf16_f32 %0, %1, %2" : "=v"(r) : "v"(lo), "v"(hi)); return r; }
; __device__ __forceinline__ float bf_lo(unsigned u) { return __uint_as_float(u << 16); }
; __device__ __forceinline__ float bf_hi(unsigned u) { return __uint_as_float(u & 0xffff0000u); }
; __device__ __forceinline__ float silu_f(float x) { return x * __builtin_amdgcn_rcpf(1.0f + __expf(-x)); }
; __device__ __forceinline__ void p4_ssd(Ctx& X, int unit) {
;     ...
;             const float dsk = XP_d_skip(X)[8 * g + e];
; #pragma unroll
;             for (int n = 0; n < 4; ++n) { const u32x2 xv = *(const LAS u32x2*)(Xh + l * 144 + (16 * n + 4 * fq) * 2), zv = zq[e2][n];
;                 const float t0_ = (y[n][0] + dsk * bf_lo(xv.x)) * silu_f(bf_lo(zv.x)), t1_ = (y[n][1] + dsk * bf_hi(xv.x)) * silu_f(bf_hi(zv.x));
;                 const float t2_ = (y[n][2] + dsk * bf_lo(xv.y)) * silu_f(bf_lo(zv.y)), t3_ = (y[n][3] + dsk * bf_hi(xv.y)) * silu_f(bf_hi(zv.y));
;                 ss += (t0_ * t0_ + t1_ * t1_) + (t2_ * t2_ + t3_ * t3_);
;                 u32x2 o; o.x = pk_bf16(t0_, t1_); o.y = pk_bf16(t2_, t3_); *(u32x2*)(op + (size_t)e * PANE_A + 16 * n) = o; }
.LBB0_633:
	s_mov_b64 s[6:7], s[98:99]
	s_or_b32 s4, s92, s12
	s_lshl_b64 s[14:15], s[4:5], 2
	v_lshlrev_b32_e32 v210, 16, v159
	v_mul_f32_e32 v117, 0xbfb8aa3b, v210
	s_waitcnt lgkmcnt(0)
	s_add_u32 s14, s6, s14
	s_addc_u32 s15, s7, s15
	global_load_dword v163, v101, s[14:15]
	v_exp_f32_e32 v117, v117
	ds_read_b64 v[208:209], v204 offset:34816
	v_lshlrev_b32_e32 v212, 16, v158
	s_lshl_b32 s4, s92, 20
	v_add_f32_e32 v117, 1.0, v117
	v_rcp_f32_e32 v162, v117
	s_waitcnt lgkmcnt(0)
	v_lshlrev_b32_e32 v211, 16, v209
	v_lshlrev_b32_e32 v213, 16, v208
	v_lshl_add_u64 v[160:161], v[118:119], 0, s[4:5]
	s_or_b32 s93, s92, 1
	s_lshl_b32 s4, s93, 9
	s_add_i32 s14, s4, 0
	s_add_i32 s14, s14, 0x1c000
	s_and_b64 vcc, exec, s[82:83]
	s_waitcnt vmcnt(0)
	v_pk_mul_f32 v[210:211], v[162:163], v[210:211]
	s_nop 0
	v_add_f32_e32 v96, v96, v211
	v_mul_f32_e32 v117, v210, v96
	v_and_b32_e32 v210, 0xffff0000, v159
	v_mul_f32_e32 v96, 0xbfb8aa3b, v210
	v_exp_f32_e32 v96, v96
	v_mov_b32_e32 v215, v163
	v_and_b32_e32 v211, 0xffff0000, v209
	v_and_b32_e32 v209, 0xffff0000, v208
	v_add_f32_e32 v96, 1.0, v96
	v_rcp_f32_e32 v162, v96
	v_mul_f32_e32 v96, 0xbfb8aa3b, v212
	v_exp_f32_e32 v96, v96
	v_and_b32_e32 v208, 0xffff0000, v158
	v_add_f32_e32 v96, 1.0, v96
	v_rcp_f32_e32 v214, v96
	v_lshlrev_b32_e32 v96, 16, v157
	v_pk_mul_f32 v[212:213], v[214:215], v[212:213]
	s_nop 0
	v_add_f32_e32 v94, v94, v213
	v_mul_f32_e32 v159, v212, v94
	v_mul_f32_e32 v94, 0xbfb8aa3b, v208
	v_exp_f32_e32 v94, v94
	v_mov_b32_e32 v213, v163
	ds_read_b128 v[214:217], v203 offset:17472
	v_add_f32_e32 v94, 1.0, v94
	v_rcp_f32_e32 v212, v94
	s_nop 0
	v_pk_mul_f32 v[208:209], v[212:213], v[208:209]
	s_nop 0
	v_add_f32_e32 v94, v95, v209
	v_mul_f32_e32 v158, v208, v94
	v_pk_mul_f32 v[94:95], v[162:163], v[210:211]
	v_mul_f32_e32 v162, 0xbfb8aa3b, v96
	v_exp_f32_e32 v162, v162
	v_add_f32_e32 v95, v97, v95
	v_mul_f32_e32 v208, v94, v95
	v_cvt_pk_bf16_f32 v94, v159, v158
	v_cvt_pk_bf16_f32 v95, v117, v208
	global_store_dwordx2 v[160:161], v[94:95], off
	ds_read_b64 v[94:95], v205 offset:34816
	v_add_f32_e32 v162, 1.0, v162
	v_rcp_f32_e32 v162, v162
	v_lshlrev_b32_e32 v210, 16, v156
	s_waitcnt lgkmcnt(0)
	v_lshlrev_b32_e32 v97, 16, v95
	v_pk_mul_f32 v[96:97], v[162:163], v[96:97]
	v_lshlrev_b32_e32 v211, 16, v94
	v_add_f32_e32 v92, v92, v97
	v_mul_f32_e32 v209, v96, v92
	v_and_b32_e32 v96, 0xffff0000, v157
	v_mul_f32_e32 v92, 0xbfb8aa3b, v96
	v_exp_f32_e32 v92, v92
	v_and_b32_e32 v97, 0xffff0000, v95
	v_and_b32_e32 v95, 0xffff0000, v94
	v_and_b32_e32 v94, 0xffff0000, v156
	v_add_f32_e32 v92, 1.0, v92
	v_rcp_f32_e32 v162, v92
	v_mul_f32_e32 v92, 0xbfb8aa3b, v210
	v_exp_f32_e32 v92, v92
	s_nop 0
	v_add_f32_e32 v92, 1.0, v92
	v_rcp_f32_e32 v212, v92
	v_lshlrev_b32_e32 v92, 16, v155
	v_pk_mul_f32 v[210:211], v[212:213], v[210:211]
	s_nop 0
	v_add_f32_e32 v90, v90, v211
	v_mul_f32_e32 v157, v210, v90
	v_mul_f32_e32 v90, 0xbfb8aa3b, v94
	v_exp_f32_e32 v90, v90
	v_mov_b32_e32 v211, v163
	v_add_f32_e32 v90, 1.0, v90
	v_rcp_f32_e32 v210, v90
	s_nop 0
	v_pk_mul_f32 v[94:95], v[210:211], v[94:95]
	s_nop 0
	v_add_f32_e32 v90, v91, v95
	v_mul_f32_e32 v156, v94, v90
	v_mul_f32_e32 v94, 0xbfb8aa3b, v92
	v_pk_mul_f32 v[90:91], v[162:163], v[96:97]
	v_exp_f32_e32 v94, v94
	v_add_f32_e32 v91, v93, v91
	v_mul_f32_e32 v210, v90, v91
	v_cvt_pk_bf16_f32 v90, v157, v156
	v_cvt_pk_bf16_f32 v91, v209, v210
	global_store_dwordx2 v[160:161], v[90:91], off offset:32
	ds_read_b64 v[90:91], v206 offset:34816
	v_add_f32_e32 v94, 1.0, v94
	v_rcp_f32_e32 v162, v94
	v_lshlrev_b32_e32 v94, 16, v154
	v_mov_b32_e32 v97, v163
	s_waitcnt lgkmcnt(0)
	v_lshlrev_b32_e32 v93, 16, v91
	v_pk_mul_f32 v[92:93], v[162:163], v[92:93]
	v_lshlrev_b32_e32 v95, 16, v90
	v_add_f32_e32 v88, v88, v93
	v_mul_f32_e32 v211, v92, v88
	v_and_b32_e32 v92, 0xffff0000, v155
	v_mul_f32_e32 v88, 0xbfb8aa3b, v92
	v_exp_f32_e32 v88, v88
	v_and_b32_e32 v93, 0xffff0000, v91
	v_and_b32_e32 v91, 0xffff0000, v90
	v_and_b32_e32 v90, 0xffff0000, v154
	v_add_f32_e32 v88, 1.0, v88
	v_rcp_f32_e32 v162, v88
	v_mul_f32_e32 v88, 0xbfb8aa3b, v94
	v_exp_f32_e32 v88, v88
	s_nop 0
	v_add_f32_e32 v88, 1.0, v88
	v_rcp_f32_e32 v96, v88
	v_lshlrev_b32_e32 v88, 16, v153
	v_pk_mul_f32 v[94:95], v[96:97], v[94:95]
	s_nop 0
	v_add_f32_e32 v86, v86, v95
	v_mul_f32_e32 v155, v94, v86
	v_mul_f32_e32 v86, 0xbfb8aa3b, v90
	v_exp_f32_e32 v86, v86
	v_mov_b32_e32 v95, v163
	v_add_f32_e32 v86, 1.0, v86
	v_rcp_f32_e32 v94, v86
	s_nop 0
	v_pk_mul_f32 v[90:91], v[94:95], v[90:91]
	s_nop 0
	v_add_f32_e32 v86, v87, v91
	v_mul_f32_e32 v154, v90, v86
	v_mul_f32_e32 v90, 0xbfb8aa3b, v88
	v_pk_mul_f32 v[86:87], v[162:163], v[92:93]
	v_exp_f32_e32 v90, v90
	v_add_f32_e32 v87, v89, v87
	v_mul_f32_e32 v212, v86, v87
	v_cvt_pk_bf16_f32 v86, v155, v154
	v_cvt_pk_bf16_f32 v87, v211, v212
	global_store_dwordx2 v[160:161], v[86:87], off offset:64
	ds_read_b64 v[86:87], v207 offset:34816
	v_add_f32_e32 v90, 1.0, v90
	v_rcp_f32_e32 v162, v90
	v_lshlrev_b32_e32 v90, 16, v152
	v_mov_b32_e32 v93, v163
	s_waitcnt lgkmcnt(0)
; #define LAS __attribute__((address_space(3)))
; __device__ __forceinline__ unsigned pk_bf16(float lo, float hi) { unsigned r; asm("v_cvt_pk_bf16_f32 %0, %1, %2" : "=v"(r) : "v"(lo), "v"(hi)); return r; }
; __device__ __forceinline__ float bf_lo(unsigned u) { return __uint_as_float(u << 16); }
; __device__ __forceinline__ void p4_ssd(Ctx& X, int unit) {
;     ...
;             for (int ks = 0; ks < 4; ++ks)
; #pragma unroll
;                 for (int n = 0; n < 4; ++n) { const bf16x8 bf = *(const LAS bf16x8*)(Ph + (16 * n + fr) * 272 + (32 * ks + 8 * fq) * 2); y[n] = mma16(bf, cfr[ks], y[n]); }
;             const float al = acS[e * 128 + l], el = __expf(al);
; #pragma unroll
;             for (int n = 0; n < 4; ++n) y[n] = y[n] * el;
; #pragma unroll
;             for (int k2 = 0; k2 < 4; ++k2) if (2 * k2 <= w) { float v[8];
; #pragma unroll
;                 for (int tq = 0; tq < 2; ++tq) { const int s0 = 16 * (2 * k2 + tq) + 4 * fq; const f32x4 as = *(const LAS f32x4*)(acS + e * 128 + s0), ds = *(const LAS f32x4*)(dtS + e * 128 + s0);
; #pragma unroll
;                     for (int j = 0; j < 4; ++j) v[4 * tq + j] = (s0 + j <= l) ? cb[2 * k2 + tq][j] * ds[j] * __expf(al - as[j]) : 0.f; }
;                 u32x4 pk; pk.x = pk_bf16(v[0], v[1]); pk.y = pk_bf16(v[2], v[3]); pk.z = pk_bf16(v[4], v[5]); pk.w = pk_bf16(v[6], v[7]);
;                 const bf16x8 gf = __builtin_bit_cast(bf16x8, pk);
; #pragma unroll
;                 for (int n = 0; n < 4; ++n) { const bf16x8 bf = tr_frag(Xh + (32 * k2) * 144 + (16 * n) * 2 + trp, 16 * 144); y[n] = mma16(bf, gf, y[n]); }
;             }
;             const float dsk = XP_d_skip(X)[8 * g + e];
; #pragma unroll
;             for (int n = 0; n < 4; ++n) { const u32x2 xv = *(const LAS u32x2*)(Xh + l * 144 + (16 * n + 4 * fq) * 2), zv = zq[e2][n];
;                 const float t0_ = (y[n][0] + dsk * bf_lo(xv.x)) * silu_f(bf_lo(zv.x)), t1_ = (y[n][1] + dsk * bf_hi(xv.x)) * silu_f(bf_hi(zv.x));
;                 const float t2_ = (y[n][2] + dsk * bf_lo(xv.y)) * silu_f(bf_lo(zv.y)), t3_ = (y[n][3] + dsk * bf_hi(xv.y)) * silu_f(bf_hi(zv.y));
;                 ss += (t0_ * t0_ + t1_ * t1_) + (t2_ * t2_ + t3_ * t3_);
;                 u32x2 o; o.x = pk_bf16(t0_, t1_); o.y = pk_bf16(t2_, t3_); *(u32x2*)(op + (size_t)e * PANE_A + 16 * n) = o; }
	v_lshlrev_b32_e32 v89, 16, v87
	v_pk_mul_f32 v[88:89], v[162:163], v[88:89]
	v_lshlrev_b32_e32 v91, 16, v86
	v_add_f32_e32 v84, v84, v89
	v_mul_f32_e32 v213, v88, v84
	v_and_b32_e32 v88, 0xffff0000, v153
	v_mul_f32_e32 v84, 0xbfb8aa3b, v88
	v_exp_f32_e32 v84, v84
	v_and_b32_e32 v89, 0xffff0000, v87
	v_and_b32_e32 v87, 0xffff0000, v86
	v_and_b32_e32 v86, 0xffff0000, v152
	v_add_f32_e32 v84, 1.0, v84
	v_rcp_f32_e32 v162, v84
	v_mul_f32_e32 v84, 0xbfb8aa3b, v90
	v_exp_f32_e32 v84, v84
	ds_read_b128 v[94:97], v203 offset:30464
	v_add_f32_e32 v84, 1.0, v84
	v_rcp_f32_e32 v92, v84
	s_nop 0
	v_pk_mul_f32 v[90:91], v[92:93], v[90:91]
	s_nop 0
	v_add_f32_e32 v82, v82, v91
	v_mul_f32_e32 v153, v90, v82
	v_mul_f32_e32 v82, 0xbfb8aa3b, v86
	v_exp_f32_e32 v82, v82
	v_mov_b32_e32 v91, v163
	v_add_f32_e32 v82, 1.0, v82
	v_rcp_f32_e32 v90, v82
	s_nop 0
	v_pk_mul_f32 v[86:87], v[90:91], v[86:87]
	s_nop 0
	v_add_f32_e32 v82, v83, v87
	v_mul_f32_e32 v152, v86, v82
	v_pk_mul_f32 v[82:83], v[162:163], v[88:89]
	ds_read_b128 v[86:89], v203 offset:21760
	v_add_f32_e32 v83, v85, v83
	v_mul_f32_e32 v162, v82, v83
	v_cvt_pk_bf16_f32 v82, v153, v152
	v_cvt_pk_bf16_f32 v83, v213, v162
	global_store_dwordx2 v[160:161], v[82:83], off offset:96
	ds_read_b128 v[82:85], v203 offset:17408
	s_waitcnt lgkmcnt(0)
	v_mfma_f32_16x16x32_bf16 v[82:85], v[82:85], v[34:37], 0
	ds_read_b128 v[90:93], v203 offset:26112
	v_lshl_add_u32 v161, v98, 2, s14
	v_add_u32_e32 v163, s4, v184
	v_mfma_f32_16x16x32_bf16 v[82:85], v[214:217], v[66:69], v[82:85]
	ds_read_b128 v[214:217], v203 offset:21824
	v_mfma_f32_16x16x32_bf16 v[86:89], v[86:89], v[34:37], 0
	s_waitcnt lgkmcnt(0)
	v_mfma_f32_16x16x32_bf16 v[86:89], v[214:217], v[66:69], v[86:89]
	ds_read_b128 v[214:217], v203 offset:26176
	v_mfma_f32_16x16x32_bf16 v[90:93], v[90:93], v[34:37], 0
	s_waitcnt lgkmcnt(0)
	v_mfma_f32_16x16x32_bf16 v[90:93], v[214:217], v[66:69], v[90:93]
	ds_read_b128 v[214:217], v203 offset:30528
	v_mfma_f32_16x16x32_bf16 v[94:97], v[94:97], v[34:37], 0
	s_waitcnt lgkmcnt(0)
	v_mfma_f32_16x16x32_bf16 v[94:97], v[214:217], v[66:69], v[94:97]
	ds_read_b128 v[214:217], v203 offset:17536
	s_waitcnt lgkmcnt(0)
	v_mfma_f32_16x16x32_bf16 v[82:85], v[214:217], v[70:73], v[82:85]
	ds_read_b128 v[214:217], v203 offset:21888
	s_waitcnt lgkmcnt(0)
	v_mfma_f32_16x16x32_bf16 v[86:89], v[214:217], v[70:73], v[86:89]
	ds_read_b128 v[214:217], v203 offset:26240
	s_waitcnt lgkmcnt(0)
	v_mfma_f32_16x16x32_bf16 v[90:93], v[214:217], v[70:73], v[90:93]
	ds_read_b128 v[214:217], v203 offset:30592
	s_waitcnt lgkmcnt(0)
	v_mfma_f32_16x16x32_bf16 v[94:97], v[214:217], v[70:73], v[94:97]
	ds_read_b128 v[214:217], v203 offset:17600
	s_waitcnt lgkmcnt(0)
	v_mfma_f32_16x16x32_bf16 v[82:85], v[214:217], v[74:77], v[82:85]
	ds_read_b128 v[214:217], v203 offset:21952
	s_waitcnt lgkmcnt(0)
	v_mfma_f32_16x16x32_bf16 v[86:89], v[214:217], v[74:77], v[86:89]
	ds_read_b128 v[214:217], v203 offset:26304
	s_waitcnt lgkmcnt(0)
	v_mfma_f32_16x16x32_bf16 v[214:217], v[214:217], v[74:77], v[90:93]
	s_nop 2
	ds_read_b128 v[90:93], v203 offset:30656
	s_waitcnt lgkmcnt(0)
	v_mfma_f32_16x16x32_bf16 v[218:221], v[90:93], v[74:77], v[94:97]
	v_lshl_add_u32 v90, v99, 2, s14
	ds_read_b32 v160, v90
	s_waitcnt lgkmcnt(0)
	v_mul_f32_e32 v90, 0x3fb8aa3b, v160
	v_exp_f32_e32 v222, v90
	s_nop 0
	v_pk_mul_f32 v[92:93], v[88:89], v[222:223] op_sel_hi:[1,0]
	v_pk_mul_f32 v[90:91], v[86:87], v[222:223] op_sel_hi:[1,0]
	v_pk_mul_f32 v[88:89], v[216:217], v[222:223] op_sel_hi:[1,0]
	v_pk_mul_f32 v[86:87], v[214:215], v[222:223] op_sel_hi:[1,0]
	ds_read_b128 v[214:217], v161
	v_pk_mul_f32 v[96:97], v[84:85], v[222:223] op_sel_hi:[1,0]
	v_pk_mul_f32 v[94:95], v[82:83], v[222:223] op_sel_hi:[1,0]
	v_pk_mul_f32 v[84:85], v[220:221], v[222:223] op_sel_hi:[1,0]
	v_pk_mul_f32 v[82:83], v[218:219], v[222:223] op_sel_hi:[1,0]
	ds_read_b128 v[218:221], v163
	s_waitcnt lgkmcnt(1)
	v_sub_f32_e32 v214, v160, v214
	v_mul_f32_e32 v214, 0x3fb8aa3b, v214
	v_exp_f32_e32 v214, v214
	v_sub_f32_e32 v215, v160, v215
	v_mul_f32_e32 v215, 0x3fb8aa3b, v215
	v_exp_f32_e32 v215, v215
	s_waitcnt lgkmcnt(0)
	v_mul_f32_e32 v218, v78, v218
	v_mul_f32_e32 v214, v218, v214
	v_cndmask_b32_e64 v222, v214, 0, s[16:17]
	v_mul_f32_e32 v214, v79, v219
	v_mul_f32_e32 v214, v214, v215
	v_sub_f32_e32 v215, v160, v216
	v_mul_f32_e32 v215, 0x3fb8aa3b, v215
	v_exp_f32_e32 v215, v215
	v_cndmask_b32_e64 v223, 0, v214, s[18:19]
	v_mul_f32_e32 v214, v80, v220
	v_mul_f32_e32 v214, v214, v215
	v_sub_f32_e32 v215, v160, v217
	v_mul_f32_e32 v215, 0x3fb8aa3b, v215
	v_exp_f32_e32 v215, v215
	v_cndmask_b32_e64 v224, v214, 0, s[20:21]
	v_mul_f32_e32 v214, v81, v221
	v_mul_f32_e32 v214, v214, v215
	v_cndmask_b32_e64 v225, v214, 0, s[22:23]
	ds_read_b128 v[214:217], v161 offset:64
	ds_read_b128 v[218:221], v163 offset:64
	s_waitcnt lgkmcnt(1)
	v_sub_f32_e32 v214, v160, v214
	v_mul_f32_e32 v214, 0x3fb8aa3b, v214
	v_exp_f32_e32 v214, v214
	v_sub_f32_e32 v215, v160, v215
	v_mul_f32_e32 v215, 0x3fb8aa3b, v215
	v_exp_f32_e32 v215, v215
	s_waitcnt lgkmcnt(0)
	v_mul_f32_e32 v218, v38, v218
	v_mul_f32_e32 v214, v218, v214
	v_cndmask_b32_e64 v218, v214, 0, s[24:25]
	v_mul_f32_e32 v214, v39, v219
	v_mul_f32_e32 v214, v214, v215
	v_sub_f32_e32 v215, v160, v216
	v_mul_f32_e32 v215, 0x3fb8aa3b, v215
	v_exp_f32_e32 v215, v215
	v_cndmask_b32_e64 v219, 0, v214, s[26:27]
	v_mul_f32_e32 v214, v40, v220
	v_cvt_pk_bf16_f32 v216, v218, v219
	v_mul_f32_e32 v214, v214, v215
	v_sub_f32_e32 v215, v160, v217
	v_mul_f32_e32 v215, 0x3fb8aa3b, v215
	v_exp_f32_e32 v215, v215
	v_cndmask_b32_e64 v220, v214, 0, s[28:29]
	v_mul_f32_e32 v214, v41, v221
	v_mul_f32_e32 v214, v214, v215
	v_cndmask_b32_e64 v217, v214, 0, s[30:31]
	v_cvt_pk_bf16_f32 v214, v222, v223
	v_cvt_pk_bf16_f32 v217, v220, v217
	ds_read_b64_tr_b16 v[220:221], v180 offset:55552
	ds_read_b64_tr_b16 v[218:219], v180 offset:53248
	ds_read_b64_tr_b16 v[222:223], v180 offset:53280
	v_cvt_pk_bf16_f32 v215, v224, v225
	ds_read_b64_tr_b16 v[224:225], v180 offset:55584
	s_waitcnt lgkmcnt(2)
	v_mfma_f32_16x16x32_bf16 v[94:97], v[218:221], v[214:217], v[94:97]
	ds_read_b64_tr_b16 v[218:219], v180 offset:53312
	ds_read_b64_tr_b16 v[220:221], v180 offset:55616
	s_waitcnt lgkmcnt(0)
	v_mfma_f32_16x16x32_bf16 v[86:89], v[218:221], v[214:217], v[86:89]
	ds_read_b64_tr_b16 v[218:219], v180 offset:53344
	ds_read_b64_tr_b16 v[220:221], v180 offset:55648
	v_mfma_f32_16x16x32_bf16 v[90:93], v[222:225], v[214:217], v[90:93]
	s_waitcnt lgkmcnt(0)
	v_mfma_f32_16x16x32_bf16 v[82:85], v[218:221], v[214:217], v[82:85]
	s_cbranch_vccz .LBB0_641
	s_and_b64 vcc, exec, s[84:85]
	s_cbranch_vccz .LBB0_642
